# pool2: slot-0 operands loaded up front, as2v operand from an LDS copy; stats2 gathers issued together
# speedup vs baseline: 1.0593x; 1.0097x over previous
.LBB3_8:
	s_or_b64 exec, exec, s[8:9]
	v_mov_b32_e32 v1, 0
	v_mov_b32_e32 v15, 0
	s_and_saveexec_b64 s[8:9], vcc
	s_waitcnt vmcnt(0)
	v_ashrrev_i32_e32 v15, 31, v14
	v_lshl_add_u64 v[14:15], v[14:15], 2, s[12:13]
	global_load_dword v15, v[14:15], off
.LBB3_10:
	s_or_b64 exec, exec, s[8:9]
	s_and_saveexec_b64 s[8:9], s[2:3]
	v_ashrrev_i32_e32 v11, 31, v10
	v_lshl_add_u64 v[10:11], v[10:11], 2, s[12:13]
	global_load_dword v1, v[10:11], off
.LBB3_12:
	s_or_b64 exec, exec, s[8:9]
	s_waitcnt vmcnt(2)
	v_mov_b32_e32 v10, 0
	v_mov_b32_e32 v11, 0
	s_and_saveexec_b64 s[8:9], s[4:5]
	v_ashrrev_i32_e32 v17, 31, v16
	v_lshl_add_u64 v[16:17], v[16:17], 2, s[12:13]
	global_load_dword v11, v[16:17], off
.LBB3_14:
	s_or_b64 exec, exec, s[8:9]
	s_and_saveexec_b64 s[8:9], s[6:7]
	v_ashrrev_i32_e32 v13, 31, v12
	v_lshl_add_u64 v[12:13], v[12:13], 2, s[12:13]
	global_load_dword v10, v[12:13], off
.LBB3_16:
	s_or_b64 exec, exec, s[8:9]
	s_waitcnt vmcnt(2)
	v_add_f32_e32 v12, v2, v15
	v_mul_f32_e32 v13, 0x3e4ccccd, v12
	v_max_f32_e32 v12, v12, v13
	v_mov_b32_e32 v13, 0xff800000
	v_add_f32_e32 v1, v2, v1
	v_cndmask_b32_e32 v15, v13, v12, vcc
	v_mul_f32_e32 v12, 0x3e4ccccd, v1
	v_max_f32_e32 v1, v1, v12
	v_cndmask_b32_e64 v16, v13, v1, s[2:3]
	s_waitcnt vmcnt(0)
	v_add_f32_e32 v1, v2, v11
	v_mul_f32_e32 v11, 0x3e4ccccd, v1
	v_max_f32_e32 v1, v1, v11
	v_cndmask_b32_e64 v17, v13, v1, s[4:5]
	v_add_f32_e32 v1, v2, v10
	v_mul_f32_e32 v10, 0x3e4ccccd, v1
	v_max_f32_e32 v1, v1, v10
	v_cndmask_b32_e64 v20, v13, v1, s[6:7]
	v_add_f32_e32 v1, v2, v3
	v_mul_f32_e32 v3, 0x3e4ccccd, v1
	v_max_f32_e32 v14, v1, v3
	v_max3_f32 v1, v16, v17, v20
	v_or_b32_e32 v10, 32, v18
	v_max3_f32 v21, v14, v15, v1
	v_cmp_lt_i32_e32 vcc, v10, v19
	s_and_saveexec_b64 s[6:7], vcc
	s_cbranch_execz .LBB3_26
	v_sub_u32_e32 v1, v9, v0
	v_subrev_u32_e32 v1, 33, v1
	v_cmp_lt_u32_e64 s[2:3], 7, v1
	s_mov_b64 s[14:15], -1
	v_mov_b32_e32 v12, v10
	s_and_saveexec_b64 s[8:9], s[2:3]
	s_cbranch_execz .LBB3_21
	v_lshrrev_b32_e32 v1, 3, v1
	v_add_u32_e32 v9, 1, v1
	v_or_b32_e32 v11, 8, v10
	v_and_b32_e32 v22, 0x3ffffffe, v9
	v_mov_b32_e32 v1, v8
	v_mov_b32_e32 v3, v2
	s_mov_b32 s20, 2
	s_mov_b64 s[16:17], 0
	s_mov_b32 s18, 0x3e4ccccd
	v_mov_b64_e32 v[12:13], v[10:11]
	v_mov_b32_e32 v11, v21

_Z12pool2_kernelPKjPKiPKfPK15HIP_vector_typeIfLj4EEPKDF16_Pfi:
	v_lshrrev_b32_e32 v74, 9, v0
	v_lshl_or_b32 v72, s2, 1, v74
	v_bfe_u32 v1, v0, 4, 2
	v_min_i32_e32 v73, 0x186, v72
	v_lshlrev_b32_e32 v123, 9, v74
	v_lshlrev_b32_e32 v75, 9, v73
	v_sub_u32_e32 v123, v123, v75
	v_add_u32_e32 v123, 0x11060, v123
	s_load_dwordx2 s[4:5], s[0:1], 0x20
	v_lshl_or_b32 v26, v73, 4, v1
	v_ashrrev_i32_e32 v27, 31, v26
	v_and_b32_e32 v90, 15, v0
	v_lshrrev_b32_e32 v2, 2, v0
	v_lshlrev_b64 v[10:11], 7, v[26:27]
	v_and_b32_e32 v91, 64, v2
	v_or_b32_e32 v16, v10, v90
	v_or_b32_e32 v10, v16, v91
	v_or_b32_e32 v42, 16, v91
	s_waitcnt lgkmcnt(0)
	v_lshl_add_u64 v[12:13], v[10:11], 4, s[4:5]
	v_or_b32_e32 v10, v16, v42
	v_or_b32_e32 v43, 32, v91
	v_lshl_add_u64 v[14:15], v[10:11], 4, s[4:5]
	v_or_b32_e32 v10, v16, v43
	v_or_b32_e32 v44, 48, v91
	global_load_dwordx4 v[2:5], v[12:13], off
	global_load_dwordx4 v[6:9], v[14:15], off
	v_lshl_add_u64 v[14:15], v[10:11], 4, s[4:5]
	v_or_b32_e32 v10, v16, v44
	v_lshl_add_u64 v[16:17], v[10:11], 4, s[4:5]
	global_load_dwordx4 v[22:25], v[14:15], off
	global_load_dwordx4 v[10:13], v[16:17], off
	v_or_b32_e32 v14, 4, v26
	v_ashrrev_i32_e32 v15, 31, v14
	v_lshlrev_b64 v[28:29], 7, v[14:15]
	v_or_b32_e32 v27, v28, v90
	v_or_b32_e32 v28, v27, v91
	v_lshl_add_u64 v[30:31], v[28:29], 4, s[4:5]
	v_or_b32_e32 v28, v27, v42
	v_lshl_add_u64 v[32:33], v[28:29], 4, s[4:5]
	global_load_dwordx4 v[14:17], v[30:31], off
	global_load_dwordx4 v[18:21], v[32:33], off
	v_or_b32_e32 v32, 8, v26
	v_ashrrev_i32_e32 v33, 31, v32
	v_or_b32_e32 v28, v27, v43
	v_lshlrev_b64 v[32:33], 7, v[32:33]
	v_lshl_add_u64 v[30:31], v[28:29], 4, s[4:5]
	v_or_b32_e32 v28, v27, v44
	v_or_b32_e32 v27, v32, v90
	v_or_b32_e32 v32, v27, v91
	v_lshl_add_u64 v[34:35], v[32:33], 4, s[4:5]
	v_or_b32_e32 v32, v27, v42
	v_lshl_add_u64 v[36:37], v[32:33], 4, s[4:5]
	v_or_b32_e32 v32, v27, v43
	v_or_b32_e32 v26, 12, v26
	v_lshl_add_u64 v[38:39], v[32:33], 4, s[4:5]
	v_or_b32_e32 v32, v27, v44
	v_ashrrev_i32_e32 v27, 31, v26
	v_lshlrev_b64 v[26:27], 7, v[26:27]
	v_or_b32_e32 v45, v26, v90
	v_or_b32_e32 v26, v45, v91
	v_lshl_add_u64 v[40:41], v[26:27], 4, s[4:5]
	v_or_b32_e32 v26, v45, v42
	v_lshl_add_u64 v[66:67], v[26:27], 4, s[4:5]
	v_or_b32_e32 v26, v45, v43
	v_lshl_add_u64 v[28:29], v[28:29], 4, s[4:5]
	v_lshl_add_u64 v[32:33], v[32:33], 4, s[4:5]
	v_lshl_add_u64 v[68:69], v[26:27], 4, s[4:5]
	v_or_b32_e32 v26, v45, v44
	v_lshl_add_u64 v[70:71], v[26:27], 4, s[4:5]
	global_load_dwordx4 v[62:65], v[30:31], off
	global_load_dwordx4 v[58:61], v[28:29], off
	global_load_dwordx4 v[46:49], v[34:35], off
	global_load_dwordx4 v[50:53], v[36:37], off
	global_load_dwordx4 v[54:57], v[38:39], off
	global_load_dwordx4 v[42:45], v[32:33], off
	s_nop 0
	global_load_dwordx4 v[26:29], v[40:41], off
	global_load_dwordx4 v[30:33], v[66:67], off
	global_load_dwordx4 v[34:37], v[68:69], off
	s_nop 0
	global_load_dwordx4 v[38:41], v[70:71], off
	s_load_dwordx4 s[8:11], s[0:1], 0x10
	s_load_dword s3, s[0:1], 0x30
	s_movk_i32 s4, 0x187
	v_and_b32_e32 v94, 0x1ff, v0
	v_cmp_gt_i32_e32 vcc, s4, v72
	v_lshlrev_b32_e32 v95, 7, v73
	s_movk_i32 s4, 0x80
	v_add_u32_e32 v70, v95, v94
	v_cmp_gt_u32_e64 s[4:5], s4, v94
	s_and_b64 s[12:13], vcc, s[4:5]
	s_waitcnt lgkmcnt(0)
	v_cmp_gt_i32_e64 s[6:7], s3, v70
	s_and_b64 s[14:15], s[12:13], s[6:7]
	v_mov_b32_e32 v69, 0
	v_mov_b32_e32 v75, 0
	v_ashrrev_i32_e32 v71, 31, v70
	v_mov_b32_e32 v96, 0
	v_mov_b32_e32 v68, 0
	v_mov_b32_e32 v66, 0
	v_mov_b32_e32 v67, 0
	s_and_saveexec_b64 s[6:7], s[14:15]
	s_cbranch_execz .LBB4_2
	v_lshl_add_u64 v[66:67], v[70:71], 4, s[10:11]
	v_lshl_add_u64 v[72:73], v[70:71], 2, s[8:9]
	global_load_dwordx4 v[66:69], v[66:67], off
	s_nop 0
	global_load_dword v96, v[72:73], off

.LBB4_8:
	s_or_b64 exec, exec, s[0:1]
	v_mov_b32_e32 v70, 0x11020
	v_lshl_add_u32 v70, v74, 5, v70
	v_lshrrev_b32_e32 v93, 6, v94
	s_and_saveexec_b64 s[6:7], s[4:5]
	s_cbranch_execz .LBB4_12
	v_mbcnt_lo_u32_b32 v72, -1, 0
	v_mbcnt_hi_u32_b32 v72, -1, v72
	v_and_b32_e32 v73, 64, v72
	s_waitcnt vmcnt(0)
	v_add_u32_e32 v75, v95, v94
	v_lshl_add_u32 v75, v75, 2, v123
	ds_write_b32 v75, v96
	v_add_u32_e32 v75, -1, v72
	v_cmp_lt_i32_e64 s[0:1], v75, v73
	v_add_u32_e32 v76, -2, v72
	s_nop 0
	v_cndmask_b32_e64 v75, v75, v72, s[0:1]
	v_lshlrev_b32_e32 v75, 2, v75
	ds_bpermute_b32 v75, v75, v71
	v_cmp_ne_u32_e64 s[0:1], 0, v92
	s_waitcnt lgkmcnt(0)
	s_nop 0
	v_cndmask_b32_e64 v75, 0, v75, s[0:1]
	v_cmp_lt_i32_e64 s[0:1], v76, v73
	v_add_u32_e32 v75, v75, v71
	s_nop 0
	v_cndmask_b32_e64 v76, v76, v72, s[0:1]
	v_lshlrev_b32_e32 v76, 2, v76
	ds_bpermute_b32 v76, v76, v75
	v_cmp_lt_u32_e64 s[0:1], 1, v92
	s_waitcnt lgkmcnt(0)
	s_nop 0
	v_cndmask_b32_e64 v76, 0, v76, s[0:1]
	v_add_u32_e32 v75, v76, v75
	v_add_u32_e32 v76, -4, v72
	v_cmp_lt_i32_e64 s[0:1], v76, v73
	s_nop 1
	v_cndmask_b32_e64 v76, v76, v72, s[0:1]
	v_lshlrev_b32_e32 v76, 2, v76
	ds_bpermute_b32 v76, v76, v75
	v_cmp_lt_u32_e64 s[0:1], 3, v92
	s_waitcnt lgkmcnt(0)
	s_nop 0
	v_cndmask_b32_e64 v76, 0, v76, s[0:1]
	v_add_u32_e32 v75, v76, v75
	v_add_u32_e32 v76, -8, v72
	v_cmp_lt_i32_e64 s[0:1], v76, v73
	s_nop 1
	v_cndmask_b32_e64 v76, v76, v72, s[0:1]
	v_lshlrev_b32_e32 v76, 2, v76
	ds_bpermute_b32 v76, v76, v75
	v_cmp_lt_u32_e64 s[0:1], 7, v92
	s_waitcnt lgkmcnt(0)
	s_nop 0
	v_cndmask_b32_e64 v76, 0, v76, s[0:1]
	v_add_u32_e32 v75, v76, v75
	v_add_u32_e32 v76, -16, v72
	v_cmp_lt_i32_e64 s[0:1], v76, v73
	s_nop 1
	v_cndmask_b32_e64 v76, v76, v72, s[0:1]
	v_lshlrev_b32_e32 v76, 2, v76
	ds_bpermute_b32 v76, v76, v75
	v_cmp_lt_u32_e64 s[0:1], 15, v92
	s_waitcnt lgkmcnt(0)
	s_nop 0
	v_cndmask_b32_e64 v76, 0, v76, s[0:1]
	v_add_u32_e32 v75, v76, v75
	v_subrev_u32_e32 v76, 32, v72
	v_cmp_lt_i32_e64 s[0:1], v76, v73
	s_nop 1
	v_cndmask_b32_e64 v72, v76, v72, s[0:1]
	v_lshlrev_b32_e32 v72, 2, v72
	ds_bpermute_b32 v72, v72, v75
	v_cmp_lt_u32_e64 s[0:1], 31, v92
	s_waitcnt lgkmcnt(0)
	s_nop 0
	v_cndmask_b32_e64 v72, 0, v72, s[0:1]
	v_add_u32_e32 v72, v72, v75
	v_cmp_eq_u32_e64 s[0:1], 63, v92
	s_and_saveexec_b64 s[18:19], s[0:1]
	v_lshl_add_u32 v73, v93, 2, v70
	ds_write_b32 v73, v72
	s_or_b64 exec, exec, s[18:19]

.LBB4_23:
	v_min_i32_e32 v71, v105, v101
	v_add_u32_e32 v109, 0x200, v105
	v_min_i32_e32 v74, v109, v101
	v_add_u32_e32 v108, 0x400, v105
	s_waitcnt lgkmcnt(0)
	v_cmp_gt_i32_e32 vcc, v102, v71
	s_waitcnt vmcnt(0)
	v_min_i32_e32 v75, v108, v101
	v_add_u32_e32 v107, 0x600, v105
	v_cndmask_b32_e64 v72, 64, 0, vcc
	v_cmp_gt_i32_e32 vcc, v102, v74
	v_min_i32_e32 v76, v107, v101
	v_add_u32_e32 v106, 0x800, v105
	v_cndmask_b32_e64 v73, 64, 0, vcc
	v_cmp_gt_i32_e32 vcc, v102, v75
	v_min_i32_e32 v70, v106, v101
	v_lshl_add_u32 v81, v72, 2, v98
	v_cndmask_b32_e64 v77, 64, 0, vcc
	v_cmp_gt_i32_e32 vcc, v102, v76
	v_lshl_add_u32 v83, v73, 2, v98
	v_lshl_add_u32 v85, v77, 2, v98
	v_cndmask_b32_e64 v78, 64, 0, vcc
	v_cmp_gt_i32_e32 vcc, v102, v70
	v_lshl_add_u32 v88, v78, 2, v98
	v_or_b32_e32 v80, 32, v72
	v_cndmask_b32_e64 v79, 64, 0, vcc
	v_lshl_add_u32 v110, v79, 2, v98
	ds_read_b32 v81, v81 offset:128
	ds_read_b32 v83, v83 offset:128
	ds_read_b32 v85, v85 offset:128
	ds_read_b32 v88, v88 offset:128
	ds_read_b32 v110, v110 offset:128
	s_waitcnt lgkmcnt(4)
	v_cmp_gt_i32_e32 vcc, v81, v71
	v_or_b32_e32 v82, 32, v73
	v_or_b32_e32 v84, 32, v77
	v_cndmask_b32_e32 v72, v80, v72, vcc
	s_waitcnt lgkmcnt(3)
	v_cmp_gt_i32_e32 vcc, v83, v74
	v_or_b32_e32 v86, 32, v78
	v_or_b32_e32 v89, 32, v79
	v_cndmask_b32_e32 v73, v82, v73, vcc
	s_waitcnt lgkmcnt(2)
	v_cmp_gt_i32_e32 vcc, v85, v75
	v_lshl_add_u32 v81, v72, 2, v98
	v_lshl_add_u32 v83, v73, 2, v98
	v_cndmask_b32_e32 v77, v84, v77, vcc
	s_waitcnt lgkmcnt(1)
	v_cmp_gt_i32_e32 vcc, v88, v76
	v_lshl_add_u32 v85, v77, 2, v98
	v_or_b32_e32 v80, 16, v72
	v_cndmask_b32_e32 v78, v86, v78, vcc
	s_waitcnt lgkmcnt(0)
	v_cmp_gt_i32_e32 vcc, v110, v70
	v_lshl_add_u32 v88, v78, 2, v98
	v_or_b32_e32 v82, 16, v73
	v_cndmask_b32_e32 v79, v89, v79, vcc
	v_lshl_add_u32 v110, v79, 2, v98
	ds_read_b32 v81, v81 offset:64
	ds_read_b32 v83, v83 offset:64
	ds_read_b32 v85, v85 offset:64
	ds_read_b32 v88, v88 offset:64
	ds_read_b32 v110, v110 offset:64
	s_waitcnt lgkmcnt(4)
	v_cmp_gt_i32_e32 vcc, v81, v71
	v_or_b32_e32 v84, 16, v77
	v_or_b32_e32 v86, 16, v78
	v_cndmask_b32_e32 v72, v80, v72, vcc
	s_waitcnt lgkmcnt(3)
	v_cmp_gt_i32_e32 vcc, v83, v74
	v_or_b32_e32 v89, 16, v79
	v_lshl_add_u32 v81, v72, 2, v98
	v_cndmask_b32_e32 v73, v82, v73, vcc
	s_waitcnt lgkmcnt(2)
	v_cmp_gt_i32_e32 vcc, v85, v75
	v_lshl_add_u32 v83, v73, 2, v98
	v_or_b32_e32 v80, 8, v72
	v_cndmask_b32_e32 v77, v84, v77, vcc
	s_waitcnt lgkmcnt(1)
	v_cmp_gt_i32_e32 vcc, v88, v76
	v_lshl_add_u32 v85, v77, 2, v98
	v_or_b32_e32 v82, 8, v73
	v_cndmask_b32_e32 v78, v86, v78, vcc
	s_waitcnt lgkmcnt(0)
	v_cmp_gt_i32_e32 vcc, v110, v70
	v_lshl_add_u32 v88, v78, 2, v98
	v_or_b32_e32 v84, 8, v77
	v_cndmask_b32_e32 v79, v89, v79, vcc
	v_lshl_add_u32 v110, v79, 2, v98
	ds_read_b32 v81, v81 offset:32
	ds_read_b32 v83, v83 offset:32
	ds_read_b32 v85, v85 offset:32
	ds_read_b32 v88, v88 offset:32
	ds_read_b32 v110, v110 offset:32
	s_waitcnt lgkmcnt(4)
	v_cmp_gt_i32_e32 vcc, v81, v71
	v_or_b32_e32 v86, 8, v78
	v_or_b32_e32 v89, 8, v79
	v_cndmask_b32_e32 v72, v80, v72, vcc
	s_waitcnt lgkmcnt(3)
	v_cmp_gt_i32_e32 vcc, v83, v74
	v_lshl_add_u32 v81, v72, 2, v98
	v_add_u32_e32 v80, 4, v72
	v_cndmask_b32_e32 v73, v82, v73, vcc
	s_waitcnt lgkmcnt(2)
	v_cmp_gt_i32_e32 vcc, v85, v75
	v_lshl_add_u32 v83, v73, 2, v98
	v_add_u32_e32 v82, 4, v73
	v_cndmask_b32_e32 v77, v84, v77, vcc
	s_waitcnt lgkmcnt(1)
	v_cmp_gt_i32_e32 vcc, v88, v76
	v_lshl_add_u32 v85, v77, 2, v98
	v_add_u32_e32 v84, 4, v77
	v_cndmask_b32_e32 v78, v86, v78, vcc
	s_waitcnt lgkmcnt(0)
	v_cmp_gt_i32_e32 vcc, v110, v70
	v_lshl_add_u32 v88, v78, 2, v98
	v_add_u32_e32 v86, 4, v78
	v_cndmask_b32_e32 v79, v89, v79, vcc
	v_lshl_add_u32 v110, v79, 2, v98
	ds_read_b32 v81, v81 offset:16
	ds_read_b32 v83, v83 offset:16
	ds_read_b32 v85, v85 offset:16
	ds_read_b32 v88, v88 offset:16
	ds_read_b32 v110, v110 offset:16
	s_waitcnt lgkmcnt(4)
	v_cmp_gt_i32_e32 vcc, v81, v71
	v_add_u32_e32 v89, 4, v79
	s_nop 0
	v_cndmask_b32_e32 v72, v80, v72, vcc
	s_waitcnt lgkmcnt(3)
	v_cmp_gt_i32_e32 vcc, v83, v74
	v_lshl_add_u32 v81, v72, 2, v98
	v_add_u32_e32 v80, 2, v72
	v_cndmask_b32_e32 v73, v82, v73, vcc
	s_waitcnt lgkmcnt(2)
	v_cmp_gt_i32_e32 vcc, v85, v75
	v_lshl_add_u32 v83, v73, 2, v98
	v_add_u32_e32 v82, 2, v73
	v_cndmask_b32_e32 v77, v84, v77, vcc
	s_waitcnt lgkmcnt(1)
	v_cmp_gt_i32_e32 vcc, v88, v76
	v_lshl_add_u32 v85, v77, 2, v98
	v_add_u32_e32 v84, 2, v77
	v_cndmask_b32_e32 v78, v86, v78, vcc
	s_waitcnt lgkmcnt(0)
	v_cmp_gt_i32_e32 vcc, v110, v70
	v_lshl_add_u32 v88, v78, 2, v98
	v_add_u32_e32 v86, 2, v78
	v_cndmask_b32_e32 v79, v89, v79, vcc
	v_lshl_add_u32 v110, v79, 2, v98
	ds_read_b32 v81, v81 offset:8
	ds_read_b32 v83, v83 offset:8
	ds_read_b32 v85, v85 offset:8
	ds_read_b32 v88, v88 offset:8
	ds_read_b32 v110, v110 offset:8
	s_waitcnt lgkmcnt(4)
	v_cmp_gt_i32_e32 vcc, v81, v71
	v_add_u32_e32 v89, 2, v79
	s_nop 0
	v_cndmask_b32_e32 v72, v80, v72, vcc
	s_waitcnt lgkmcnt(3)
	v_cmp_gt_i32_e32 vcc, v83, v74
	v_lshl_add_u32 v81, v72, 2, v98
	v_add_u32_e32 v80, 1, v72
	v_cndmask_b32_e32 v73, v82, v73, vcc
	s_waitcnt lgkmcnt(2)
	v_cmp_gt_i32_e32 vcc, v85, v75
	v_lshl_add_u32 v83, v73, 2, v98
	v_add_u32_e32 v82, 1, v73
	v_cndmask_b32_e32 v77, v84, v77, vcc
	s_waitcnt lgkmcnt(1)
	v_cmp_gt_i32_e32 vcc, v88, v76
	v_lshl_add_u32 v85, v77, 2, v98
	v_add_u32_e32 v84, 1, v77
	v_cndmask_b32_e32 v78, v86, v78, vcc
	s_waitcnt lgkmcnt(0)
	v_cmp_gt_i32_e32 vcc, v110, v70
	v_lshl_add_u32 v88, v78, 2, v98
	v_add_u32_e32 v86, 1, v78
	v_cndmask_b32_e32 v79, v89, v79, vcc
	v_lshl_add_u32 v110, v79, 2, v98
	ds_read_b32 v81, v81 offset:4
	ds_read_b32 v83, v83 offset:4
	ds_read_b32 v85, v85 offset:4
	ds_read_b32 v88, v88 offset:4
	ds_read_b32 v110, v110 offset:4
	s_waitcnt lgkmcnt(4)
	v_cmp_gt_i32_e32 vcc, v81, v71
	v_add_u32_e32 v89, 1, v79
	s_nop 0
	v_cndmask_b32_e32 v72, v80, v72, vcc
	s_waitcnt lgkmcnt(3)
	v_cmp_gt_i32_e32 vcc, v83, v74
	v_lshlrev_b32_e32 v72, 2, v72
	v_add_u32_e32 v80, v97, v72
	v_cndmask_b32_e32 v73, v82, v73, vcc
	s_waitcnt lgkmcnt(2)
	v_cmp_gt_i32_e32 vcc, v85, v75
	v_lshlrev_b32_e32 v73, 2, v73
	v_add_u32_e32 v72, v98, v72
	v_cndmask_b32_e32 v77, v84, v77, vcc
	s_waitcnt lgkmcnt(1)
	v_cmp_gt_i32_e32 vcc, v88, v76
	v_lshlrev_b32_e32 v77, 2, v77
	v_add_u32_e32 v81, v97, v73
	v_cndmask_b32_e32 v78, v86, v78, vcc
	v_lshlrev_b32_e32 v78, 2, v78
	v_add_u32_e32 v82, v97, v77
	v_add_u32_e32 v77, v98, v77
	v_add_u32_e32 v83, v97, v78
	v_add_u32_e32 v78, v98, v78
	v_add_u32_e32 v73, v98, v73
	ds_read_b32 v80, v80
	ds_read_b32 v72, v72
	ds_read_b32 v81, v81
	ds_read_b32 v84, v73
	ds_read_b32 v82, v82
	ds_read_b32 v77, v77
	ds_read_b32 v83, v83
	ds_read_b32 v78, v78
	s_waitcnt lgkmcnt(7)
	v_add_u32_e32 v71, v80, v71
	s_waitcnt lgkmcnt(6)
	v_sub_u32_e32 v72, v71, v72
	v_ashrrev_i32_e32 v73, 31, v72
	v_lshl_add_u64 v[72:73], v[72:73], 2, s[16:17]
	s_waitcnt lgkmcnt(5)
	v_add_u32_e32 v71, v81, v74
	global_load_dword v116, v[72:73], off
	s_waitcnt lgkmcnt(4)
	v_sub_u32_e32 v72, v71, v84
	v_ashrrev_i32_e32 v73, 31, v72
	v_lshl_add_u64 v[72:73], v[72:73], 2, s[16:17]
	s_waitcnt lgkmcnt(3)
	v_add_u32_e32 v71, v82, v75
	global_load_dword v114, v[72:73], off
	s_waitcnt lgkmcnt(2)
	v_sub_u32_e32 v72, v71, v77
	v_cmp_gt_i32_e32 vcc, v110, v70
	v_ashrrev_i32_e32 v73, 31, v72
	v_lshl_add_u64 v[72:73], v[72:73], 2, s[16:17]
	v_cndmask_b32_e32 v79, v89, v79, vcc
	s_waitcnt lgkmcnt(1)
	v_add_u32_e32 v71, v83, v76
	global_load_dword v112, v[72:73], off
	s_waitcnt lgkmcnt(0)
	v_sub_u32_e32 v72, v71, v78
	v_lshlrev_b32_e32 v71, 2, v79
	v_add_u32_e32 v73, v97, v71
	v_add_u32_e32 v71, v98, v71
	ds_read_b32 v74, v73
	ds_read_b32 v71, v71
	v_ashrrev_i32_e32 v73, 31, v72
	v_lshl_add_u64 v[72:73], v[72:73], 2, s[16:17]
	global_load_dword v111, v[72:73], off
	s_waitcnt lgkmcnt(1)
	v_add_u32_e32 v70, v74, v70
	s_waitcnt lgkmcnt(0)
	v_sub_u32_e32 v70, v70, v71
	v_ashrrev_i32_e32 v71, 31, v70
	v_lshl_add_u64 v[70:71], v[70:71], 2, s[16:17]
	global_load_dword v110, v[70:71], off
	s_waitcnt vmcnt(4)
	v_lshlrev_b32_sdwa v88, v103, v116 dst_sel:DWORD dst_unused:UNUSED_PAD src0_sel:DWORD src1_sel:WORD_0
	v_add_u32_sdwa v86, v116, v95 dst_sel:DWORD dst_unused:UNUSED_PAD src0_sel:WORD_1 src1_sel:DWORD
	v_lshl_add_u32 v86, v86, 2, v123
	ds_read_b32 v119, v86
	global_load_dwordx4 v[124:127], v88, s[10:11]
	s_waitcnt vmcnt(4)
	v_lshlrev_b32_sdwa v70, v103, v114 dst_sel:DWORD dst_unused:UNUSED_PAD src0_sel:DWORD src1_sel:WORD_0
	v_add_u32_sdwa v86, v114, v95 dst_sel:DWORD dst_unused:UNUSED_PAD src0_sel:WORD_1 src1_sel:DWORD
	global_load_dwordx4 v[82:85], v70, s[10:11]
	v_lshl_add_u32 v86, v86, 2, v123
	ds_read_b32 v118, v86
	s_waitcnt vmcnt(4)
	v_lshlrev_b32_sdwa v70, v103, v112 dst_sel:DWORD dst_unused:UNUSED_PAD src0_sel:DWORD src1_sel:WORD_0
	v_add_u32_sdwa v86, v112, v95 dst_sel:DWORD dst_unused:UNUSED_PAD src0_sel:WORD_1 src1_sel:DWORD
	global_load_dwordx4 v[78:81], v70, s[10:11]
	v_lshl_add_u32 v86, v86, 2, v123
	ds_read_b32 v117, v86
	s_waitcnt vmcnt(4)
	v_lshlrev_b32_sdwa v70, v103, v111 dst_sel:DWORD dst_unused:UNUSED_PAD src0_sel:DWORD src1_sel:WORD_0
	v_add_u32_sdwa v86, v111, v95 dst_sel:DWORD dst_unused:UNUSED_PAD src0_sel:WORD_1 src1_sel:DWORD
	global_load_dwordx4 v[74:77], v70, s[10:11]
	v_lshl_add_u32 v86, v86, 2, v123
	ds_read_b32 v115, v86
	s_waitcnt vmcnt(4)
	v_add_u32_sdwa v86, v110, v95 dst_sel:DWORD dst_unused:UNUSED_PAD src0_sel:WORD_1 src1_sel:DWORD
	v_lshl_add_u32 v86, v86, 2, v123
	ds_read_b32 v113, v86
	v_lshlrev_b32_sdwa v70, v103, v110 dst_sel:DWORD dst_unused:UNUSED_PAD src0_sel:DWORD src1_sel:WORD_0
	global_load_dwordx4 v[70:73], v70, s[10:11]
	s_waitcnt vmcnt(4) lgkmcnt(4)
	v_cmp_gt_u32_e32 vcc, 64, v127
	s_and_saveexec_b64 s[0:1], vcc
	s_cbranch_execz .LBB4_25
	v_lshlrev_b32_sdwa v89, v104, v116 dst_sel:DWORD dst_unused:UNUSED_PAD src0_sel:DWORD src1_sel:WORD_1
	v_add_f32_e32 v86, v119, v124
	v_mul_f32_e32 v88, 0x3e4ccccd, v86
	v_max_f32_e32 v86, v86, v88
	v_sub_f32_e32 v86, v86, v125
	v_exp_f32_e32 v86, v86
	v_mul_lo_u32 v88, v127, s3
	v_add3_u32 v88, v99, v88, v89
	v_mul_f32_e32 v86, v126, v86
	ds_add_f32 v88, v86
.LBB4_25:
	s_or_b64 exec, exec, s[0:1]
	v_cmp_lt_i32_e32 vcc, v109, v100
	s_waitcnt vmcnt(3)
	v_cmp_gt_u32_e64 s[0:1], 64, v85
	s_and_b64 s[18:19], vcc, s[0:1]
	s_and_saveexec_b64 s[0:1], s[18:19]
	s_cbranch_execz .LBB4_27
	s_waitcnt lgkmcnt(3)
	v_add_f32_e32 v82, v118, v82
	v_mul_f32_e32 v86, 0x3e4ccccd, v82
	v_max_f32_e32 v82, v82, v86
	v_sub_f32_e32 v82, v82, v83
	v_exp_f32_e32 v82, v82
	v_mul_lo_u32 v83, v85, s3
	v_lshlrev_b32_sdwa v85, v104, v114 dst_sel:DWORD dst_unused:UNUSED_PAD src0_sel:DWORD src1_sel:WORD_1
	v_add3_u32 v83, v99, v83, v85
	v_mul_f32_e32 v82, v84, v82
	ds_add_f32 v83, v82
.LBB4_27:
	s_or_b64 exec, exec, s[0:1]
	v_cmp_lt_i32_e32 vcc, v108, v100
	s_waitcnt vmcnt(2)
	v_cmp_gt_u32_e64 s[0:1], 64, v81
	s_and_b64 s[18:19], vcc, s[0:1]
	s_and_saveexec_b64 s[0:1], s[18:19]
	s_cbranch_execz .LBB4_29
	s_waitcnt lgkmcnt(2)
	v_add_f32_e32 v78, v117, v78
	v_mul_f32_e32 v82, 0x3e4ccccd, v78
	v_max_f32_e32 v78, v78, v82
	v_sub_f32_e32 v78, v78, v79
	v_exp_f32_e32 v78, v78
	v_mul_lo_u32 v79, v81, s3
	v_lshlrev_b32_sdwa v81, v104, v112 dst_sel:DWORD dst_unused:UNUSED_PAD src0_sel:DWORD src1_sel:WORD_1
	v_add3_u32 v79, v99, v79, v81
	v_mul_f32_e32 v78, v80, v78
	ds_add_f32 v79, v78
.LBB4_29:
	s_or_b64 exec, exec, s[0:1]
	v_cmp_lt_i32_e32 vcc, v107, v100
	s_waitcnt vmcnt(1)
	v_cmp_gt_u32_e64 s[0:1], 64, v77
	s_and_b64 s[18:19], vcc, s[0:1]
	s_and_saveexec_b64 s[0:1], s[18:19]
	s_cbranch_execz .LBB4_31
	s_waitcnt lgkmcnt(1)
	v_add_f32_e32 v74, v115, v74
	v_mul_f32_e32 v78, 0x3e4ccccd, v74
	v_max_f32_e32 v74, v74, v78
	v_sub_f32_e32 v74, v74, v75
	v_exp_f32_e32 v74, v74
	v_mul_lo_u32 v75, v77, s3
	v_lshlrev_b32_sdwa v77, v104, v111 dst_sel:DWORD dst_unused:UNUSED_PAD src0_sel:DWORD src1_sel:WORD_1
	v_add3_u32 v75, v99, v75, v77
	v_mul_f32_e32 v74, v76, v74
	ds_add_f32 v75, v74
.LBB4_31:
	s_or_b64 exec, exec, s[0:1]
	v_cmp_lt_i32_e32 vcc, v106, v100
	s_waitcnt vmcnt(0) lgkmcnt(0)
	v_cmp_gt_u32_e64 s[0:1], 64, v73
	s_and_b64 s[18:19], vcc, s[0:1]
	s_and_saveexec_b64 s[0:1], s[18:19]
	s_cbranch_execz .LBB4_22
	v_add_f32_e32 v70, v113, v70
	v_mul_f32_e32 v74, 0x3e4ccccd, v70
	v_max_f32_e32 v70, v70, v74
	v_sub_f32_e32 v70, v70, v71
	v_exp_f32_e32 v70, v70
	v_mul_lo_u32 v71, v73, s3
	v_lshlrev_b32_sdwa v73, v104, v110 dst_sel:DWORD dst_unused:UNUSED_PAD src0_sel:DWORD src1_sel:WORD_1
	v_add3_u32 v71, v99, v71, v73
	v_mul_f32_e32 v70, v72, v70
	ds_add_f32 v71, v70
	s_branch .LBB4_22

	.amdhsa_kernel _Z12pool2_kernelPKjPKiPKfPK15HIP_vector_typeIfLj4EEPKDF16_Pfi
		.amdhsa_group_segment_fixed_size 70752
		.amdhsa_private_segment_fixed_size 0
		.amdhsa_kernarg_size 52
		.amdhsa_user_sgpr_count 2
		.amdhsa_user_sgpr_dispatch_ptr 0
		.amdhsa_user_sgpr_queue_ptr 0
		.amdhsa_user_sgpr_kernarg_segment_ptr 1
		.amdhsa_user_sgpr_dispatch_id 0
		.amdhsa_user_sgpr_kernarg_preload_length 0
		.amdhsa_user_sgpr_kernarg_preload_offset 0
		.amdhsa_user_sgpr_private_segment_size 0
		.amdhsa_uses_dynamic_stack 0
		.amdhsa_enable_private_segment 0
		.amdhsa_system_sgpr_workgroup_id_x 1
		.amdhsa_system_sgpr_workgroup_id_y 0
		.amdhsa_system_sgpr_workgroup_id_z 0
		.amdhsa_system_sgpr_workgroup_info 0
		.amdhsa_system_vgpr_workitem_id 0
		.amdhsa_next_free_vgpr 128
		.amdhsa_next_free_sgpr 20
		.amdhsa_accum_offset 128
		.amdhsa_reserve_vcc 1
		.amdhsa_float_round_mode_32 0
		.amdhsa_float_round_mode_16_64 0
		.amdhsa_float_denorm_mode_32 3
		.amdhsa_float_denorm_mode_16_64 3
		.amdhsa_dx10_clamp 1
		.amdhsa_ieee_mode 1
		.amdhsa_fp16_overflow 0
		.amdhsa_tg_split 0
		.amdhsa_exception_fp_ieee_invalid_op 0
		.amdhsa_exception_fp_denorm_src 0
		.amdhsa_exception_fp_ieee_div_zero 0
		.amdhsa_exception_fp_ieee_overflow 0
		.amdhsa_exception_fp_ieee_underflow 0
		.amdhsa_exception_fp_ieee_inexact 0
		.amdhsa_exception_int_div_zero 0
	.end_amdhsa_kernel

amdhsa.kernels:
  - .agpr_count:     0
    .args:
      - .actual_access:  read_only
        .address_space:  global
        .offset:         0
        .size:           8
        .value_kind:     global_buffer
      - .actual_access:  read_only
        .address_space:  global
        .offset:         8
        .size:           8
        .value_kind:     global_buffer
      - .actual_access:  read_only
        .address_space:  global
        .offset:         16
        .size:           8
        .value_kind:     global_buffer
      - .actual_access:  read_only
        .address_space:  global
        .offset:         24
        .size:           8
        .value_kind:     global_buffer
      - .actual_access:  read_only
        .address_space:  global
        .offset:         32
        .size:           8
        .value_kind:     global_buffer
      - .actual_access:  read_only
        .address_space:  global
        .offset:         40
        .size:           8
        .value_kind:     global_buffer
      - .actual_access:  read_only
        .address_space:  global
        .offset:         48
        .size:           8
        .value_kind:     global_buffer
      - .actual_access:  read_only
        .address_space:  global
        .offset:         56
        .size:           8
        .value_kind:     global_buffer
      - .actual_access:  read_only
        .address_space:  global
        .offset:         64
        .size:           8
        .value_kind:     global_buffer
      - .actual_access:  read_only
        .address_space:  global
        .offset:         72
        .size:           8
        .value_kind:     global_buffer
      - .actual_access:  read_only
        .address_space:  global
        .offset:         80
        .size:           8
        .value_kind:     global_buffer
      - .actual_access:  read_only
        .address_space:  global
        .offset:         88
        .size:           8
        .value_kind:     global_buffer
      - .actual_access:  read_only
        .address_space:  global
        .offset:         96
        .size:           8
        .value_kind:     global_buffer
      - .actual_access:  write_only
        .address_space:  global
        .offset:         104
        .size:           8
        .value_kind:     global_buffer
      - .actual_access:  write_only
        .address_space:  global
        .offset:         112
        .size:           8
        .value_kind:     global_buffer
      - .actual_access:  write_only
        .address_space:  global
        .offset:         120
        .size:           8
        .value_kind:     global_buffer
      - .actual_access:  write_only
        .address_space:  global
        .offset:         128
        .size:           8
        .value_kind:     global_buffer
      - .actual_access:  write_only
        .address_space:  global
        .offset:         136
        .size:           8
        .value_kind:     global_buffer
      - .actual_access:  write_only
        .address_space:  global
        .offset:         144
        .size:           8
        .value_kind:     global_buffer
      - .actual_access:  write_only
        .address_space:  global
        .offset:         152
        .size:           8
        .value_kind:     global_buffer
      - .actual_access:  write_only
        .address_space:  global
        .offset:         160
        .size:           8
        .value_kind:     global_buffer
      - .actual_access:  write_only
        .address_space:  global
        .offset:         168
        .size:           8
        .value_kind:     global_buffer
      - .actual_access:  read_only
        .address_space:  global
        .offset:         176
        .size:           8
        .value_kind:     global_buffer
    .group_segment_fixed_size: 29696
    .kernarg_segment_align: 8
    .kernarg_segment_size: 184
    .language:       OpenCL C
    .language_version:
      - 2
      - 0
    .max_flat_workgroup_size: 512
    .name:           _Z12front_kernelPKiS0_PKfS2_S2_S2_S2_S2_S2_S2_S2_S2_S2_PjS3_PiS4_PDF16_PfS6_S4_S5_S0_
    .private_segment_fixed_size: 0
    .sgpr_count:     30
    .sgpr_spill_count: 0
    .symbol:         _Z12front_kernelPKiS0_PKfS2_S2_S2_S2_S2_S2_S2_S2_S2_S2_PjS3_PiS4_PDF16_PfS6_S4_S5_S0_.kd
    .uniform_work_group_size: 1
    .uses_dynamic_stack: false
    .vgpr_count:     80
    .vgpr_spill_count: 0
    .wavefront_size: 64
  - .agpr_count:     0
    .args:
      - .actual_access:  read_only
        .address_space:  global
        .offset:         0
        .size:           8
        .value_kind:     global_buffer
      - .actual_access:  read_only
        .address_space:  global
        .offset:         8
        .size:           8
        .value_kind:     global_buffer
      - .actual_access:  write_only
        .address_space:  global
        .offset:         16
        .size:           8
        .value_kind:     global_buffer
      - .actual_access:  write_only
        .address_space:  global
        .offset:         24
        .size:           8
        .value_kind:     global_buffer
      - .actual_access:  write_only
        .address_space:  global
        .offset:         32
        .size:           8
        .value_kind:     global_buffer
      - .actual_access:  read_only
        .address_space:  global
        .offset:         40
        .size:           8
        .value_kind:     global_buffer
      - .actual_access:  read_only
        .address_space:  global
        .offset:         48
        .size:           8
        .value_kind:     global_buffer
      - .actual_access:  write_only
        .address_space:  global
        .offset:         56
        .size:           8
        .value_kind:     global_buffer
      - .actual_access:  write_only
        .address_space:  global
        .offset:         64
        .size:           8
        .value_kind:     global_buffer
    .group_segment_fixed_size: 40960
    .kernarg_segment_align: 8
    .kernarg_segment_size: 72
    .language:       OpenCL C
    .language_version:
      - 2
      - 0
    .max_flat_workgroup_size: 512
    .name:           _Z13second_kernelPKfPKDF16_PDF16_PfS4_PKjPKiPiS9_
    .private_segment_fixed_size: 0
    .sgpr_count:     29
    .sgpr_spill_count: 0
    .symbol:         _Z13second_kernelPKfPKDF16_PDF16_PfS4_PKjPKiPiS9_.kd
    .uniform_work_group_size: 1
    .uses_dynamic_stack: false
    .vgpr_count:     64
    .vgpr_spill_count: 0
    .wavefront_size: 64
  - .agpr_count:     0
    .args:
      - .actual_access:  read_only
        .address_space:  global
        .offset:         0
        .size:           8
        .value_kind:     global_buffer
      - .actual_access:  read_only
        .address_space:  global
        .offset:         8
        .size:           8
        .value_kind:     global_buffer
      - .actual_access:  read_only
        .address_space:  global
        .offset:         16
        .size:           8
        .value_kind:     global_buffer
      - .actual_access:  read_only
        .address_space:  global
        .offset:         24
        .size:           8
        .value_kind:     global_buffer
      - .actual_access:  read_only
        .address_space:  global
        .offset:         32
        .size:           8
        .value_kind:     global_buffer
      - .actual_access:  read_only
        .address_space:  global
        .offset:         40
        .size:           8
        .value_kind:     global_buffer
      - .actual_access:  read_only
        .address_space:  global
        .offset:         48
        .size:           8
        .value_kind:     global_buffer
      - .actual_access:  write_only
        .address_space:  global
        .offset:         56
        .size:           8
        .value_kind:     global_buffer
      - .actual_access:  write_only
        .address_space:  global
        .offset:         64
        .size:           8
        .value_kind:     global_buffer
      - .actual_access:  write_only
        .address_space:  global
        .offset:         72
        .size:           8
        .value_kind:     global_buffer
      - .offset:         80
        .size:           4
        .value_kind:     by_value
    .group_segment_fixed_size: 10240
    .kernarg_segment_align: 8
    .kernarg_segment_size: 84
    .language:       OpenCL C
    .language_version:
      - 2
      - 0
    .max_flat_workgroup_size: 256
    .name:           _Z11agg1_kernelPKDF16_PKfS2_PKiS4_S2_S2_PDF16_PfS6_i
    .private_segment_fixed_size: 0
    .sgpr_count:     50
    .sgpr_spill_count: 0
    .symbol:         _Z11agg1_kernelPKDF16_PKfS2_PKiS4_S2_S2_PDF16_PfS6_i.kd
    .uniform_work_group_size: 1
    .uses_dynamic_stack: false
    .vgpr_count:     70
    .vgpr_spill_count: 0
    .wavefront_size: 64
  - .agpr_count:     0
    .args:
      - .actual_access:  read_only
        .address_space:  global
        .offset:         0
        .size:           8
        .value_kind:     global_buffer
      - .actual_access:  read_only
        .address_space:  global
        .offset:         8
        .size:           8
        .value_kind:     global_buffer
      - .actual_access:  read_only
        .address_space:  global
        .offset:         16
        .size:           8
        .value_kind:     global_buffer
      - .actual_access:  read_only
        .address_space:  global
        .offset:         24
        .size:           8
        .value_kind:     global_buffer
      - .actual_access:  read_only
        .address_space:  global
        .offset:         32
        .size:           8
        .value_kind:     global_buffer
      - .actual_access:  write_only
        .address_space:  global
        .offset:         40
        .size:           8
        .value_kind:     global_buffer
      - .offset:         48
        .size:           4
        .value_kind:     by_value
    .group_segment_fixed_size: 0
    .kernarg_segment_align: 8
    .kernarg_segment_size: 52
    .language:       OpenCL C
    .language_version:
      - 2
      - 0
    .max_flat_workgroup_size: 256
    .name:           _Z13stats2_kernelPKiS0_PKfS2_S0_P15HIP_vector_typeIfLj4EEi
    .private_segment_fixed_size: 0
    .sgpr_count:     27
    .sgpr_spill_count: 0
    .symbol:         _Z13stats2_kernelPKiS0_PKfS2_S0_P15HIP_vector_typeIfLj4EEi.kd
    .uniform_work_group_size: 1
    .uses_dynamic_stack: false
    .vgpr_count:     32
    .vgpr_spill_count: 0
    .wavefront_size: 64
  - .agpr_count:     0
    .args:
      - .actual_access:  read_only
        .address_space:  global
        .offset:         0
        .size:           8
        .value_kind:     global_buffer
      - .actual_access:  read_only
        .address_space:  global
        .offset:         8
        .size:           8
        .value_kind:     global_buffer
      - .actual_access:  read_only
        .address_space:  global
        .offset:         16
        .size:           8
        .value_kind:     global_buffer
      - .actual_access:  read_only
        .address_space:  global
        .offset:         24
        .size:           8
        .value_kind:     global_buffer
      - .actual_access:  read_only
        .address_space:  global
        .offset:         32
        .size:           8
        .value_kind:     global_buffer
      - .actual_access:  write_only
        .address_space:  global
        .offset:         40
        .size:           8
        .value_kind:     global_buffer
      - .offset:         48
        .size:           4
        .value_kind:     by_value
    .group_segment_fixed_size: 70752
    .kernarg_segment_align: 8
    .kernarg_segment_size: 52
    .language:       OpenCL C
    .language_version:
      - 2
      - 0
    .max_flat_workgroup_size: 1024
    .name:           _Z12pool2_kernelPKjPKiPKfPK15HIP_vector_typeIfLj4EEPKDF16_Pfi
    .private_segment_fixed_size: 0
    .sgpr_count:     26
    .sgpr_spill_count: 0
    .symbol:         _Z12pool2_kernelPKjPKiPKfPK15HIP_vector_typeIfLj4EEPKDF16_Pfi.kd
    .uniform_work_group_size: 1
    .uses_dynamic_stack: false
    .vgpr_count:     128
    .vgpr_spill_count: 0
    .wavefront_size: 64
  - .agpr_count:     0
    .args:
      - .actual_access:  read_only
        .address_space:  global
        .offset:         0
        .size:           8
        .value_kind:     global_buffer
      - .actual_access:  read_only
        .address_space:  global
        .offset:         8
        .size:           8
        .value_kind:     global_buffer
      - .actual_access:  read_only
        .address_space:  global
        .offset:         16
        .size:           8
        .value_kind:     global_buffer
      - .actual_access:  read_only
        .address_space:  global
        .offset:         24
        .size:           8
        .value_kind:     global_buffer
      - .actual_access:  read_only
        .address_space:  global
        .offset:         32
        .size:           8
        .value_kind:     global_buffer
      - .actual_access:  read_only
        .address_space:  global
        .offset:         40
        .size:           8
        .value_kind:     global_buffer
      - .actual_access:  read_only
        .address_space:  global
        .offset:         48
        .size:           8
        .value_kind:     global_buffer
      - .actual_access:  read_only
        .address_space:  global
        .offset:         56
        .size:           8
        .value_kind:     global_buffer
      - .actual_access:  write_only
        .address_space:  global
        .offset:         64
        .size:           8
        .value_kind:     global_buffer
    .group_segment_fixed_size: 9472
    .kernarg_segment_align: 8
    .kernarg_segment_size: 72
    .language:       OpenCL C
    .language_version:
      - 2
      - 0
    .max_flat_workgroup_size: 1024
    .name:           _Z10mlp_kernelPKfPKiS0_S0_S0_S0_S0_S0_Pf
    .private_segment_fixed_size: 0
    .sgpr_count:     76
    .sgpr_spill_count: 0
    .symbol:         _Z10mlp_kernelPKfPKiS0_S0_S0_S0_S0_S0_Pf.kd
    .uniform_work_group_size: 1
    .uses_dynamic_stack: false
    .vgpr_count:     77
    .vgpr_spill_count: 0
    .wavefront_size: 64
